# v59 + s_waitcnt vmcnt(0) at the tile-loop head of the six fp8 GEMM calls (epilogue stores drained before the next tile's load segments)
# baseline (speedup 1.0000x reference)
; template <class Epi, class Sched, bool ALIGN_EPI = true, bool F8 = false>
; __device__ __forceinline__ void gemm_phase(PG8_LAS unsigned char* lds, const Sched& S, const Epi& E) {
;     ...
;     for (;;) {
;         const bool has_next = S.next(ui + 1, nxt);
;         const char* nA = has_next ? nxt.A : cA; const char* nB = has_next ? nxt.B : cB;
;         const int nt = cur.nt;
; #pragma unroll 1
;         for (int t = 0; t < nt; t += 2) {
;     ...
;         cur = nxt; cA = nA; cB = nB; ++ui;
.LBB0_368:
	s_waitcnt vmcnt(0)
	s_andn2_b64 vcc, exec, s[0:1]
	s_mov_b32 s4, s20
	s_mov_b32 s66, s18
	s_mov_b64 s[26:27], s[22:23]
	s_mov_b64 s[28:29], s[24:25]
	s_cbranch_vccz .LBB0_410

; template <class Epi, class Sched, bool ALIGN_EPI = true, bool F8 = false>
; __device__ __forceinline__ void gemm_phase(PG8_LAS unsigned char* lds, const Sched& S, const Epi& E) {
;     ...
;     for (;;) {
;         const bool has_next = S.next(ui + 1, nxt);
;         const char* nA = has_next ? nxt.A : cA; const char* nB = has_next ? nxt.B : cB;
;         const int nt = cur.nt;
; #pragma unroll 1
;         for (int t = 0; t < nt; t += 2) {
.LBB0_420:
	s_waitcnt vmcnt(0)
	s_andn2_b64 vcc, exec, s[0:1]
	s_mov_b32 s8, s18
	s_mov_b32 s73, s16
	s_mov_b64 s[24:25], s[20:21]
	s_mov_b64 s[26:27], s[22:23]
	s_cbranch_vccz .LBB0_434

; template <class Epi, class Sched, bool ALIGN_EPI = true, bool F8 = false>
; __device__ __forceinline__ void gemm_phase(PG8_LAS unsigned char* lds, const Sched& S, const Epi& E) {
;     ...
;     for (;;) {
;         const bool has_next = S.next(ui + 1, nxt);
;         const char* nA = has_next ? nxt.A : cA; const char* nB = has_next ? nxt.B : cB;
;         const int nt = cur.nt;
; #pragma unroll 1
;         for (int t = 0; t < nt; t += 2) {
.LBB0_826:
	s_waitcnt vmcnt(0)
	s_and_b64 vcc, exec, s[0:1]
	s_mov_b32 s70, s67
	s_mov_b32 s71, s68
	s_mov_b32 s72, s69
	s_mov_b32 s73, s66
	s_mov_b64 s[24:25], s[20:21]
	s_mov_b64 s[26:27], s[22:23]
	s_cbranch_vccnz .LBB0_846

; template <class Epi, class Sched, bool ALIGN_EPI = true, bool F8 = false>
; __device__ __forceinline__ void gemm_phase(PG8_LAS unsigned char* lds, const Sched& S, const Epi& E) {
;     ...
;     for (;;) {
;         const bool has_next = S.next(ui + 1, nxt);
;         const char* nA = has_next ? nxt.A : cA; const char* nB = has_next ? nxt.B : cB;
;         const int nt = cur.nt;
; #pragma unroll 1
;         for (int t = 0; t < nt; t += 2) {
.LBB0_903:
	s_waitcnt vmcnt(0)
	s_andn2_b64 vcc, exec, s[0:1]
	s_mov_b32 s26, s20
	s_mov_b32 s64, s18
	s_mov_b64 s[28:29], s[22:23]
	s_mov_b64 s[30:31], s[24:25]
	s_cbranch_vccz .LBB0_917

; template <class Epi, class Sched, bool ALIGN_EPI = true, bool F8 = false>
; __device__ __forceinline__ void gemm_phase(PG8_LAS unsigned char* lds, const Sched& S, const Epi& E) {
;     ...
;     for (;;) {
;         const bool has_next = S.next(ui + 1, nxt);
;         const char* nA = has_next ? nxt.A : cA; const char* nB = has_next ? nxt.B : cB;
;         const int nt = cur.nt;
; #pragma unroll 1
;         for (int t = 0; t < nt; t += 2) {
.LBB0_1052:
	s_waitcnt vmcnt(0)
	s_andn2_b64 vcc, exec, s[22:23]
	s_cbranch_vccz .LBB0_1075

; template <class Epi, class Sched, bool ALIGN_EPI = true, bool F8 = false>
; __device__ __forceinline__ void gemm_phase(PG8_LAS unsigned char* lds, const Sched& S, const Epi& E) {
;     ...
;     for (;;) {
;         const bool has_next = S.next(ui + 1, nxt);
;         const char* nA = has_next ? nxt.A : cA; const char* nB = has_next ? nxt.B : cB;
;         const int nt = cur.nt;
; #pragma unroll 1
;         for (int t = 0; t < nt; t += 2) {
.LBB0_1132:
	s_waitcnt vmcnt(0)
	s_andn2_b64 vcc, exec, s[20:21]
	s_mov_b32 s66, s64
	s_mov_b32 s22, s60
	s_mov_b32 s65, s62
	s_mov_b32 s48, s63
	s_mov_b64 s[24:25], s[16:17]
	s_mov_b64 s[26:27], s[18:19]
	s_cbranch_vccz .LBB0_1160
